# strategy 8 (MFMA shadow fill): RWKV chain consumer's loop-tail address updates moved into the issue gaps of the last five MFMAs
# speedup vs baseline: 1.0068x; 1.0068x over previous
; #define LAS __attribute__((address_space(3)))
; DI unsigned cvt2(float lo, float hi) { return __builtin_bit_cast(unsigned, __builtin_convertvector((f32x2){lo, hi}, bfv2)); }
; DI void phase_chain(const Frame& F) {
;     ...
;             for (int jj = 0; jj < NSUB; ++jj) {
;                 __builtin_amdgcn_s_barrier(); asm volatile("" ::: "memory");
;                 const LAS unsigned char* st = ring + cur * CH_STB;
;                 bf16x8 sb[4]; sb[0] = pack8(S0, 0); sb[1] = pack8(S0, 1); sb[2] = pack8(S1, 0); sb[3] = pack8(S1, 1);
;                 const bf16x8 vt = *(const LAS bf16x8*)(st + 12800 + r * 32 + h * 16), wh = *(const LAS bf16x8*)(st + 12288 + rs * 32 + h * 16);
;                 const bf16x8 kh0 = *(const LAS bf16x8*)(st + 8192 + r * 32 + h * 16), kh1 = *(const LAS bf16x8*)(st + 8192 + (32 + r) * 32 + h * 16);
;                 f32x16 Y, N0, N1;
; #pragma unroll
;                 for (int i = 0; i < 16; ++i) { Y[i] = 0.f; N0[i] = 0.f; N1[i] = 0.f; }
;                 Y = __builtin_amdgcn_mfma_f32_32x32x16_bf16(wh, vt, Y, 0, 0, 0);
;                 N0 = __builtin_amdgcn_mfma_f32_32x32x16_bf16(kh0, vt, N0, 0, 0, 0);
;                 N1 = __builtin_amdgcn_mfma_f32_32x32x16_bf16(kh1, vt, N1, 0, 0, 0);
; #pragma unroll
;                 for (int ks = 0; ks < 4; ++ks) { const int c0 = ((4 * ks + h) ^ rs) * 8, c1 = ((4 * ks + h + 2) ^ rs) * 8;
;                     Y = __builtin_amdgcn_mfma_f32_32x32x16_bf16(cat8(st + 10240 + rs * 128 + c0, st + 10240 + rs * 128 + c1), sb[ks], Y, 0, 0, 0);
;                     N0 = __builtin_amdgcn_mfma_f32_32x32x16_bf16(cat8(st + r * 128 + c0, st + r * 128 + c1), sb[ks], N0, 0, 0, 0);
;                     N1 = __builtin_amdgcn_mfma_f32_32x32x16_bf16(cat8(st + (32 + r) * 128 + c0, st + (32 + r) * 128 + c1), sb[ks], N1, 0, 0, 0); }
;                 S0 = N0; S1 = N1;
; #pragma unroll
;                 for (int q = 0; q < 8; q += 1) { const int t = (q & 3) + 8 * (q >> 2) + 4 * h; *(LAS bf16_t*)(ybuf + (t * 32 + r) * 2) = (bf16_t)(cvt2(Y[q], 0.f) & 0xffffu); }
;                 { const u32x4 w = *(const LAS u32x4*)(ybuf + F.lane * 16); const int t = F.lane >> 2, step = 16 * jj + t, tt = d ? (SEQ - 1 - step) : step;
;                   *(u32x4*)(YD + ((size_t)d * T + (size_t)b * SEQ + tt) * 512 + hd * 64 + 32 * rb + 8 * (F.lane & 3)) = w; }
;                 cur = cur == CH_NST - 1 ? 0 : cur + 1;
.Lchain_nostore:
	v_mfma_f32_32x32x16_bf16 v[32:47], v[134:137], v[138:141], 0
	ds_read_b64 v[154:155], v213
	ds_read_b64 v[156:157], v214
	v_add_u32_e32 v215, v131, v83
	v_add_u32_e32 v216, v131, v84
	ds_read_b64 v[158:159], v215
	ds_read_b64 v[160:161], v216
	v_add_u32_e32 v215, v129, v85
	v_add_u32_e32 v216, v129, v86
	ds_read_b64 v[162:163], v215 offset:10240
	ds_read_b64 v[164:165], v216 offset:10240
	s_waitcnt lgkmcnt(9)
	v_mfma_f32_32x32x16_bf16 v[16:31], v[142:145], v[138:141], 0
	v_add_u32_e32 v215, v130, v85
	v_add_u32_e32 v216, v130, v86
	ds_read_b64 v[166:167], v215
	ds_read_b64 v[168:169], v216
	s_waitcnt lgkmcnt(10)
	v_mfma_f32_32x32x16_bf16 v[0:15], v[146:149], v[138:141], 0
	v_add_u32_e32 v215, v131, v85
	v_add_u32_e32 v216, v131, v86
	ds_read_b64 v[170:171], v215
	ds_read_b64 v[172:173], v216
	s_waitcnt lgkmcnt(10)
	v_mfma_f32_32x32x16_bf16 v[32:47], v[150:153], v[102:105], v[32:47]
	v_add_u32_e32 v215, v129, v87
	v_add_u32_e32 v216, v129, v88
	ds_read_b64 v[174:175], v215 offset:10240
	ds_read_b64 v[176:177], v216 offset:10240
	s_waitcnt lgkmcnt(10)
	v_mfma_f32_32x32x16_bf16 v[16:31], v[154:157], v[102:105], v[16:31]
	v_add_u32_e32 v215, v130, v87
	v_add_u32_e32 v216, v130, v88
	ds_read_b64 v[178:179], v215
	ds_read_b64 v[180:181], v216
	s_waitcnt lgkmcnt(10)
	v_mfma_f32_32x32x16_bf16 v[0:15], v[158:161], v[102:105], v[0:15]
	v_add_u32_e32 v215, v131, v87
	v_add_u32_e32 v216, v131, v88
	ds_read_b64 v[182:183], v215
	ds_read_b64 v[184:185], v216
	s_waitcnt lgkmcnt(10)
	v_mfma_f32_32x32x16_bf16 v[32:47], v[162:165], v[106:109], v[32:47]
	v_add_u32_e32 v215, v129, v89
	v_add_u32_e32 v216, v129, v90
	ds_read_b64 v[194:195], v215 offset:10240
	ds_read_b64 v[196:197], v216 offset:10240
	s_waitcnt lgkmcnt(10)
	v_mfma_f32_32x32x16_bf16 v[16:31], v[166:169], v[106:109], v[16:31]
	v_add_u32_e32 v215, v130, v89
	v_add_u32_e32 v216, v130, v90
	ds_read_b64 v[198:199], v215
	ds_read_b64 v[200:201], v216
	s_waitcnt lgkmcnt(10)
	v_mfma_f32_32x32x16_bf16 v[0:15], v[170:173], v[106:109], v[0:15]
	v_add_u32_e32 v215, v131, v89
	v_add_u32_e32 v216, v131, v90
	ds_read_b64 v[202:203], v215
	ds_read_b64 v[204:205], v216
	s_waitcnt lgkmcnt(10)
	v_mfma_f32_32x32x16_bf16 v[32:47], v[174:177], v[52:55], v[32:47]
	s_add_i32 s2, s5, 1
	s_cmp_lg_u32 s5, 5
	s_cselect_b32 s5, s2, 0
	s_mul_i32 s2, s5, 0x3800
	v_add3_u32 v126, s2, v78, v77
	s_waitcnt lgkmcnt(8)
	v_mfma_f32_32x32x16_bf16 v[16:31], v[178:181], v[52:55], v[16:31]
	v_add3_u32 v127, s2, v76, v77
	v_add3_u32 v128, s2, v79, v77
	v_add_u32_e32 v129, s2, v80
	v_add_u32_e32 v130, s2, v81
	v_add_u32_e32 v131, s2, v82
	s_waitcnt lgkmcnt(6)
	v_mfma_f32_32x32x16_bf16 v[0:15], v[182:185], v[52:55], v[0:15]
	v_add_u32_e32 v132, v129, v83
	v_add_u32_e32 v212, v129, v84
	v_add_u32_e32 v213, v130, v83
	v_add_u32_e32 v214, v130, v84
	s_waitcnt lgkmcnt(4)
	v_mfma_f32_32x32x16_bf16 v[32:47], v[194:197], v[48:51], v[32:47]
	v_add_u32_e32 v217, s4, v92
	s_add_i32 s4, s4, -16
	v_cndmask_b32_e32 v210, v217, v101, vcc
	v_ashrrev_i32_e32 v211, 31, v210
	v_lshl_add_u64 v[210:211], s[52:53], 0, v[210:211]
	s_waitcnt lgkmcnt(2)
	v_mfma_f32_32x32x16_bf16 v[16:31], v[198:201], v[48:51], v[16:31]
	v_add_u32_e32 v101, 16, v101
	v_lshlrev_b64 v[210:211], 10, v[210:211]
	v_lshl_add_u64 v[210:211], v[74:75], 0, v[210:211]
	v_add_u32_e32 v217, 0x15000, v56
	s_waitcnt lgkmcnt(0)
	v_mfma_f32_32x32x16_bf16 v[0:15], v[202:205], v[48:51], v[0:15]
	s_nop 2
	v_cvt_pk_bf16_f32 v32, v32, s0
	v_cvt_pk_bf16_f32 v33, v33, s0
	v_cvt_pk_bf16_f32 v34, v34, s0
	v_cvt_pk_bf16_f32 v35, v35, s0
	v_cvt_pk_bf16_f32 v36, v36, s0
	v_cvt_pk_bf16_f32 v37, v37, s0
	v_cvt_pk_bf16_f32 v38, v38, s0
	v_cvt_pk_bf16_f32 v39, v39, s0
	ds_write_b16 v93, v32
	ds_write_b16 v94, v33
	ds_write_b16 v95, v34
	ds_write_b16 v96, v35
	ds_write_b16 v97, v36
	ds_write_b16 v98, v37
	ds_write_b16 v99, v38
	ds_write_b16 v100, v39
	ds_read_b128 v[206:209], v217
	s_cmp_eq_u32 s4, -1
	s_cbranch_scc0 .LBB0_756
	s_waitcnt lgkmcnt(0)
	global_store_dwordx4 v[210:211], v[206:209], off
	s_waitcnt vmcnt(0)
	s_waitcnt lgkmcnt(0)
	s_mov_b64 s[4:5], 0
	s_barrier
